# speedup vs baseline: 1.0026x; 1.0026x over previous
_Z5k_decPKiPKDF16_S2_PKfS4_S4_Pf:
	s_load_dword s3, s[0:1], 0x44
	s_load_dword s6, s[0:1], 0x38
	s_load_dwordx2 s[4:5], s[0:1], 0x0
	s_load_dwordx8 s[28:35], s[0:1], 0x8
	s_load_dwordx4 s[12:15], s[0:1], 0x28
	v_and_b32_e32 v1, 15, v0
	v_and_b32_e32 v64, 63, v0
	v_lshlrev_b32_e32 v96, 3, v1
	v_lshrrev_b32_e32 v4, 3, v0
	v_and_b32_e32 v4, 4, v4
	v_or_b32_e32 v96, v96, v4
	v_mov_b32_e32 v97, 0
	v_and_b32_e32 v104, 16, v0
	v_lshlrev_b32_e32 v6, 7, v0
	v_lshlrev_b32_e32 v7, 2, v64
	s_movk_i32 s16, 0x6000
	v_and_or_b32 v103, v6, s16, v7
	v_mov_b32_e32 v219, 0
	s_movk_i32 s19, 0x3d08
	s_waitcnt lgkmcnt(0)
	s_and_b32 s3, s3, 0xffff
	s_mul_i32 s2, s2, s3
	v_add_u32_e32 v5, s2, v0
	s_mul_i32 s6, s6, s3
	v_lshrrev_b32_e32 v102, 6, v5
	s_lshr_b32 s18, s6, 6
	v_readfirstlane_b32 s23, v102
	v_lshl_add_u64 v[2:3], s[4:5], 0, v[96:97]
	s_mov_b32 s16, 0xf4240
	v_cmp_gt_u32_e32 vcc, s16, v5
	s_and_saveexec_b64 s[22:23], vcc
	s_cbranch_execz .LBB2_3
	v_mov_b32_e32 v222, v2
	v_mov_b32_e32 v223, v3
	v_min_u32_e32 v218, s19, v102
	v_lshlrev_b32_e32 v218, 9, v218
	v_lshl_add_u64 v[216:217], v[222:223], 0, v[218:219]
	global_load_dword v65, v[216:217], off nt
	global_load_dword v80, v[216:217], off offset:128 nt
	global_load_dword v81, v[216:217], off offset:256 nt
	global_load_dword v82, v[216:217], off offset:384 nt
	v_add_u32_e32 v220, s18, v102
	v_min_u32_e32 v218, s19, v220
	v_lshlrev_b32_e32 v218, 9, v218
	v_lshl_add_u64 v[216:217], v[222:223], 0, v[218:219]
	global_load_dword v100, v[216:217], off nt
	global_load_dword v101, v[216:217], off offset:128 nt
	global_load_dword v98, v[216:217], off offset:256 nt
	global_load_dword v99, v[216:217], off offset:384 nt
	s_mov_b32 s8, s28
	s_and_b32 s9, s29, 0xffff
	s_mov_b32 s10, 0x30d400
	s_mov_b32 s11, 0x20000
	s_mov_b64 s[36:37], 0x1000
	v_and_b32_e32 v96, 48, v64
	v_lshlrev_b32_e32 v221, 6, v1
	v_lshlrev_b32_e32 v211, 2, v1
	v_lshlrev_b32_e32 v214, 4, v0
	v_add_u32_e32 v215, 0x1000, v214
	v_lshl_add_u32 v134, v1, 6, v96
	v_add_u32_e32 v134, 0x9000, v134
	v_add_u32_e32 v133, 0x9000, v214
	v_lshl_or_b32 v221, v102, 6, v64
	v_lshrrev_b32_e32 v213, 4, v64
	v_cmp_gt_u32_e32 vcc, 16, v64
	v_and_b32_e32 v210, 31, v64
	v_lshlrev_b32_e32 v210, 4, v210
	s_mov_b32 s38, -1
	s_mov_b32 s39, 0
	s_mov_b64 exec, s[38:39]
	global_load_dwordx4 v[126:129], v210, s[32:33]
	s_mov_b32 s38, 0
	s_mov_b32 s39, -1
	s_mov_b64 exec, s[38:39]
	global_load_dwordx4 v[126:129], v210, s[34:35]
	s_mov_b64 exec, -1
	global_load_dwordx4 v[32:35], v214, s[30:31]
	global_load_dwordx4 v[36:39], v215, s[30:31]
	s_load_dword s12, s[12:13], 0x0
	s_waitcnt vmcnt(8)
	v_lshl_or_b32 v216, v65, 5, v104
	v_lshl_or_b32 v217, v80, 5, v104
	v_lshl_or_b32 v218, v81, 5, v104
	v_lshl_or_b32 v212, v82, 5, v104
	buffer_load_dwordx4 v[92:95], v216, s[8:11], 0 offen
	buffer_load_dwordx4 v[88:91], v217, s[8:11], 0 offen
	buffer_load_dwordx4 v[84:87], v218, s[8:11], 0 offen
	buffer_load_dwordx4 v[80:83], v212, s[8:11], 0 offen
	s_lshl_b32 s21, s18, 6
	s_mov_b32 s20, 2
	s_mov_b64 s[16:17], 0
	v_cmp_eq_u32_e64 s[0:1], 1, v213
	v_cmp_eq_u32_e64 s[2:3], 2, v213
	v_cmp_eq_u32_e64 s[4:5], 3, v213
	v_mov_b32_e32 v96, v221
	v_mov_b32_e32 v97, 0
	s_waitcnt vmcnt(6)
	v_lshrrev_b32_e32 v210, 6, v0
	v_lshlrev_b32_e32 v210, 10, v210
	v_add_u32_e32 v210, 0x8000, v210
	v_lshl_add_u32 v130, v64, 4, v210
	v_lshl_add_u32 v131, v213, 4, v210
	v_add_u32_e32 v132, v211, v210
	ds_write_b128 v130, v[126:129]
	ds_read_b128 v[68:71], v131 offset:512
	ds_read_b128 v[72:75], v131 offset:576
	ds_read_b128 v[76:79], v131 offset:640
	ds_read_b128 v[106:109], v131 offset:704
	ds_read_b128 v[110:113], v131 offset:768
	ds_read_b128 v[114:117], v131 offset:832
	ds_read_b128 v[118:121], v131 offset:896
	ds_read_b128 v[122:125], v131 offset:960
	s_waitcnt lgkmcnt(0)
	s_waitcnt vmcnt(4)
	ds_write_b128 v133, v[32:35]
	ds_write_b128 v133, v[36:39] offset:4096
	ds_read_b32 v148, v132 offset:512
	ds_read_b32 v149, v132 offset:576
	ds_read_b32 v150, v132 offset:640
	ds_read_b32 v151, v132 offset:704
	ds_read_b32 v152, v132 offset:768
	ds_read_b32 v153, v132 offset:832
	ds_read_b32 v154, v132 offset:896
	ds_read_b32 v155, v132 offset:960
	ds_read_b32 v156, v132 offset:0
	ds_read_b32 v157, v132 offset:64
	ds_read_b32 v158, v132 offset:128
	ds_read_b32 v159, v132 offset:192
	s_waitcnt lgkmcnt(0)
	ds_read_b32 v160, v132 offset:256
	ds_read_b32 v161, v132 offset:320
	ds_read_b32 v162, v132 offset:384
	ds_read_b32 v163, v132 offset:448
	ds_read_b128 v[0:3], v131 offset:0
	ds_read_b128 v[4:7], v131 offset:64
	ds_read_b128 v[8:11], v131 offset:128
	ds_read_b128 v[12:15], v131 offset:192
	ds_read_b128 v[16:19], v131 offset:256
	ds_read_b128 v[20:23], v131 offset:320
	ds_read_b128 v[24:27], v131 offset:384
	ds_read_b128 v[28:31], v131 offset:448
	s_waitcnt lgkmcnt(0)
	s_barrier
	ds_read_b128 v[32:35], v134
	ds_read_b128 v[36:39], v134 offset:1024
	ds_read_b128 v[40:43], v134 offset:2048
	ds_read_b128 v[44:47], v134 offset:3072
	ds_read_b128 v[48:51], v134 offset:4096
	ds_read_b128 v[52:55], v134 offset:5120
	ds_read_b128 v[56:59], v134 offset:6144
	ds_read_b128 v[60:63], v134 offset:7168
	v_cvt_pk_f16_f32 v67, v74, v75
	v_cvt_pk_f16_f32 v66, v72, v73
	v_cvt_pk_f16_f32 v65, v70, v71
	v_cvt_pk_f16_f32 v64, v68, v69
	v_cvt_pk_f16_f32 v71, v108, v109
	v_cvt_pk_f16_f32 v70, v106, v107
	v_cvt_pk_f16_f32 v69, v78, v79
	v_cvt_pk_f16_f32 v68, v76, v77
	v_cvt_pk_f16_f32 v75, v116, v117
	v_cvt_pk_f16_f32 v74, v114, v115
	v_cvt_pk_f16_f32 v73, v112, v113
	v_cvt_pk_f16_f32 v72, v110, v111
	v_cvt_pk_f16_f32 v79, v124, v125
	v_cvt_pk_f16_f32 v78, v122, v123
	v_cvt_pk_f16_f32 v77, v120, v121
	v_cvt_pk_f16_f32 v76, v118, v119
	v_mov_b32_e32 v167, 0x38003800
	v_pk_mul_f16 v64, v64, v167
	v_pk_mul_f16 v65, v65, v167
	v_pk_mul_f16 v66, v66, v167
	v_pk_mul_f16 v67, v67, v167
	v_pk_mul_f16 v68, v68, v167
	v_pk_mul_f16 v69, v69, v167
	v_pk_mul_f16 v70, v70, v167
	v_pk_mul_f16 v71, v71, v167
	v_pk_mul_f16 v72, v72, v167
	v_pk_mul_f16 v73, v73, v167
	v_pk_mul_f16 v74, v74, v167
	v_pk_mul_f16 v75, v75, v167
	v_pk_mul_f16 v76, v76, v167
	v_pk_mul_f16 v77, v77, v167
	v_pk_mul_f16 v78, v78, v167
	v_pk_mul_f16 v79, v79, v167
	v_cvt_f16_f32_e32 v148, v148
	v_cvt_f16_f32_e32 v149, v149
	v_cvt_f16_f32_e32 v150, v150
	v_cvt_f16_f32_e32 v151, v151
	v_cvt_f16_f32_e32 v152, v152
	v_cvt_f16_f32_e32 v153, v153
	v_cvt_f16_f32_e32 v154, v154
	v_cvt_f16_f32_e32 v155, v155
	v_cvt_f32_f16_e32 v148, v148
	v_cvt_f32_f16_e32 v149, v149
	v_cvt_f32_f16_e32 v150, v150
	v_cvt_f32_f16_e32 v151, v151
	v_cvt_f32_f16_e32 v152, v152
	v_cvt_f32_f16_e32 v153, v153
	v_cvt_f32_f16_e32 v154, v154
	v_cvt_f32_f16_e32 v155, v155
	v_mul_f32_e32 v148, 0.5, v148
	v_mul_f32_e32 v149, 0.5, v149
	v_mul_f32_e32 v150, 0.5, v150
	v_mul_f32_e32 v151, 0.5, v151
	v_mul_f32_e32 v152, 0.5, v152
	v_mul_f32_e32 v153, 0.5, v153
	v_mul_f32_e32 v154, 0.5, v154
	v_mul_f32_e32 v155, 0.5, v155
	v_mov_b32_e32 v140, 0
	v_mov_b32_e32 v141, 0
	v_mov_b32_e32 v142, 0
	v_mov_b32_e32 v143, 0
	v_mov_b32_e32 v144, 0
	v_mov_b32_e32 v145, 0
	v_mov_b32_e32 v146, 0
	v_mov_b32_e32 v147, 0
	v_mov_b32_e32 v166, 0
	s_waitcnt lgkmcnt(0)
	v_cvt_f32_f16_e32 v164, v32
	v_cvt_f32_f16_sdwa v165, v32 dst_sel:DWORD dst_unused:UNUSED_PAD src0_sel:WORD_1
	v_fmac_f32_e32 v140, v148, v164
	v_fmac_f32_e32 v141, v148, v165
	v_cvt_f32_f16_e32 v164, v33
	v_cvt_f32_f16_sdwa v165, v33 dst_sel:DWORD dst_unused:UNUSED_PAD src0_sel:WORD_1
	v_fmac_f32_e32 v142, v148, v164
	v_fmac_f32_e32 v143, v148, v165
	v_cvt_f32_f16_e32 v164, v34
	v_cvt_f32_f16_sdwa v165, v34 dst_sel:DWORD dst_unused:UNUSED_PAD src0_sel:WORD_1
	v_fmac_f32_e32 v144, v148, v164
	v_fmac_f32_e32 v145, v148, v165
	v_cvt_f32_f16_e32 v164, v35
	v_cvt_f32_f16_sdwa v165, v35 dst_sel:DWORD dst_unused:UNUSED_PAD src0_sel:WORD_1
	v_fmac_f32_e32 v146, v148, v164
	v_fmac_f32_e32 v147, v148, v165
	v_fmac_f32_e32 v166, v148, v156
	v_cvt_f32_f16_e32 v164, v36
	v_cvt_f32_f16_sdwa v165, v36 dst_sel:DWORD dst_unused:UNUSED_PAD src0_sel:WORD_1
	v_fmac_f32_e32 v140, v149, v164
	v_fmac_f32_e32 v141, v149, v165
	v_cvt_f32_f16_e32 v164, v37
	v_cvt_f32_f16_sdwa v165, v37 dst_sel:DWORD dst_unused:UNUSED_PAD src0_sel:WORD_1
	v_fmac_f32_e32 v142, v149, v164
	v_fmac_f32_e32 v143, v149, v165
	v_cvt_f32_f16_e32 v164, v38
	v_cvt_f32_f16_sdwa v165, v38 dst_sel:DWORD dst_unused:UNUSED_PAD src0_sel:WORD_1
	v_fmac_f32_e32 v144, v149, v164
	v_fmac_f32_e32 v145, v149, v165
	v_cvt_f32_f16_e32 v164, v39
	v_cvt_f32_f16_sdwa v165, v39 dst_sel:DWORD dst_unused:UNUSED_PAD src0_sel:WORD_1
	v_fmac_f32_e32 v146, v149, v164
	v_fmac_f32_e32 v147, v149, v165
	v_fmac_f32_e32 v166, v149, v157
	v_cvt_f32_f16_e32 v164, v40
	v_cvt_f32_f16_sdwa v165, v40 dst_sel:DWORD dst_unused:UNUSED_PAD src0_sel:WORD_1
	v_fmac_f32_e32 v140, v150, v164
	v_fmac_f32_e32 v141, v150, v165
	v_cvt_f32_f16_e32 v164, v41
	v_cvt_f32_f16_sdwa v165, v41 dst_sel:DWORD dst_unused:UNUSED_PAD src0_sel:WORD_1
	v_fmac_f32_e32 v142, v150, v164
	v_fmac_f32_e32 v143, v150, v165
	v_cvt_f32_f16_e32 v164, v42
	v_cvt_f32_f16_sdwa v165, v42 dst_sel:DWORD dst_unused:UNUSED_PAD src0_sel:WORD_1
	v_fmac_f32_e32 v144, v150, v164
	v_fmac_f32_e32 v145, v150, v165
	v_cvt_f32_f16_e32 v164, v43
	v_cvt_f32_f16_sdwa v165, v43 dst_sel:DWORD dst_unused:UNUSED_PAD src0_sel:WORD_1
	v_fmac_f32_e32 v146, v150, v164
	v_fmac_f32_e32 v147, v150, v165
	v_fmac_f32_e32 v166, v150, v158
	v_cvt_f32_f16_e32 v164, v44
	v_cvt_f32_f16_sdwa v165, v44 dst_sel:DWORD dst_unused:UNUSED_PAD src0_sel:WORD_1
	v_fmac_f32_e32 v140, v151, v164
	v_fmac_f32_e32 v141, v151, v165
	v_cvt_f32_f16_e32 v164, v45
	v_cvt_f32_f16_sdwa v165, v45 dst_sel:DWORD dst_unused:UNUSED_PAD src0_sel:WORD_1
	v_fmac_f32_e32 v142, v151, v164
	v_fmac_f32_e32 v143, v151, v165
	v_cvt_f32_f16_e32 v164, v46
	v_cvt_f32_f16_sdwa v165, v46 dst_sel:DWORD dst_unused:UNUSED_PAD src0_sel:WORD_1
	v_fmac_f32_e32 v144, v151, v164
	v_fmac_f32_e32 v145, v151, v165
	v_cvt_f32_f16_e32 v164, v47
	v_cvt_f32_f16_sdwa v165, v47 dst_sel:DWORD dst_unused:UNUSED_PAD src0_sel:WORD_1
	v_fmac_f32_e32 v146, v151, v164
	v_fmac_f32_e32 v147, v151, v165
	v_fmac_f32_e32 v166, v151, v159
	v_cvt_f32_f16_e32 v164, v48
	v_cvt_f32_f16_sdwa v165, v48 dst_sel:DWORD dst_unused:UNUSED_PAD src0_sel:WORD_1
	v_fmac_f32_e32 v140, v152, v164
	v_fmac_f32_e32 v141, v152, v165
	v_cvt_f32_f16_e32 v164, v49
	v_cvt_f32_f16_sdwa v165, v49 dst_sel:DWORD dst_unused:UNUSED_PAD src0_sel:WORD_1
	v_fmac_f32_e32 v142, v152, v164
	v_fmac_f32_e32 v143, v152, v165
	v_cvt_f32_f16_e32 v164, v50
	v_cvt_f32_f16_sdwa v165, v50 dst_sel:DWORD dst_unused:UNUSED_PAD src0_sel:WORD_1
	v_fmac_f32_e32 v144, v152, v164
	v_fmac_f32_e32 v145, v152, v165
	v_cvt_f32_f16_e32 v164, v51
	v_cvt_f32_f16_sdwa v165, v51 dst_sel:DWORD dst_unused:UNUSED_PAD src0_sel:WORD_1
	v_fmac_f32_e32 v146, v152, v164
	v_fmac_f32_e32 v147, v152, v165
	v_fmac_f32_e32 v166, v152, v160
	v_cvt_f32_f16_e32 v164, v52
	v_cvt_f32_f16_sdwa v165, v52 dst_sel:DWORD dst_unused:UNUSED_PAD src0_sel:WORD_1
	v_fmac_f32_e32 v140, v153, v164
	v_fmac_f32_e32 v141, v153, v165
	v_cvt_f32_f16_e32 v164, v53
	v_cvt_f32_f16_sdwa v165, v53 dst_sel:DWORD dst_unused:UNUSED_PAD src0_sel:WORD_1
	v_fmac_f32_e32 v142, v153, v164
	v_fmac_f32_e32 v143, v153, v165
	v_cvt_f32_f16_e32 v164, v54
	v_cvt_f32_f16_sdwa v165, v54 dst_sel:DWORD dst_unused:UNUSED_PAD src0_sel:WORD_1
	v_fmac_f32_e32 v144, v153, v164
	v_fmac_f32_e32 v145, v153, v165
	v_cvt_f32_f16_e32 v164, v55
	v_cvt_f32_f16_sdwa v165, v55 dst_sel:DWORD dst_unused:UNUSED_PAD src0_sel:WORD_1
	v_fmac_f32_e32 v146, v153, v164
	v_fmac_f32_e32 v147, v153, v165
	v_fmac_f32_e32 v166, v153, v161
	v_cvt_f32_f16_e32 v164, v56
	v_cvt_f32_f16_sdwa v165, v56 dst_sel:DWORD dst_unused:UNUSED_PAD src0_sel:WORD_1
	v_fmac_f32_e32 v140, v154, v164
	v_fmac_f32_e32 v141, v154, v165
	v_cvt_f32_f16_e32 v164, v57
	v_cvt_f32_f16_sdwa v165, v57 dst_sel:DWORD dst_unused:UNUSED_PAD src0_sel:WORD_1
	v_fmac_f32_e32 v142, v154, v164
	v_fmac_f32_e32 v143, v154, v165
	v_cvt_f32_f16_e32 v164, v58
	v_cvt_f32_f16_sdwa v165, v58 dst_sel:DWORD dst_unused:UNUSED_PAD src0_sel:WORD_1
	v_fmac_f32_e32 v144, v154, v164
	v_fmac_f32_e32 v145, v154, v165
	v_cvt_f32_f16_e32 v164, v59
	v_cvt_f32_f16_sdwa v165, v59 dst_sel:DWORD dst_unused:UNUSED_PAD src0_sel:WORD_1
	v_fmac_f32_e32 v146, v154, v164
	v_fmac_f32_e32 v147, v154, v165
	v_fmac_f32_e32 v166, v154, v162
	v_cvt_f32_f16_e32 v164, v60
	v_cvt_f32_f16_sdwa v165, v60 dst_sel:DWORD dst_unused:UNUSED_PAD src0_sel:WORD_1
	v_fmac_f32_e32 v140, v155, v164
	v_fmac_f32_e32 v141, v155, v165
	v_cvt_f32_f16_e32 v164, v61
	v_cvt_f32_f16_sdwa v165, v61 dst_sel:DWORD dst_unused:UNUSED_PAD src0_sel:WORD_1
	v_fmac_f32_e32 v142, v155, v164
	v_fmac_f32_e32 v143, v155, v165
	v_cvt_f32_f16_e32 v164, v62
	v_cvt_f32_f16_sdwa v165, v62 dst_sel:DWORD dst_unused:UNUSED_PAD src0_sel:WORD_1
	v_fmac_f32_e32 v144, v155, v164
	v_fmac_f32_e32 v145, v155, v165
	v_cvt_f32_f16_e32 v164, v63
	v_cvt_f32_f16_sdwa v165, v63 dst_sel:DWORD dst_unused:UNUSED_PAD src0_sel:WORD_1
	v_fmac_f32_e32 v146, v155, v164
	v_fmac_f32_e32 v147, v155, v165
	v_fmac_f32_e32 v166, v155, v163
	v_add_f32_dpp v140, v140, v140 row_ror:8 row_mask:0xf bank_mask:0xf
	v_add_f32_dpp v141, v141, v141 row_ror:8 row_mask:0xf bank_mask:0xf
	v_add_f32_dpp v142, v142, v142 row_ror:8 row_mask:0xf bank_mask:0xf
	v_add_f32_dpp v143, v143, v143 row_ror:8 row_mask:0xf bank_mask:0xf
	v_add_f32_dpp v144, v144, v144 row_ror:8 row_mask:0xf bank_mask:0xf
	v_add_f32_dpp v145, v145, v145 row_ror:8 row_mask:0xf bank_mask:0xf
	v_add_f32_dpp v146, v146, v146 row_ror:8 row_mask:0xf bank_mask:0xf
	v_add_f32_dpp v147, v147, v147 row_ror:8 row_mask:0xf bank_mask:0xf
	v_add_f32_dpp v166, v166, v166 row_ror:8 row_mask:0xf bank_mask:0xf
	v_add_f32_dpp v140, v140, v140 row_ror:4 row_mask:0xf bank_mask:0xf
	v_add_f32_dpp v141, v141, v141 row_ror:4 row_mask:0xf bank_mask:0xf
	v_add_f32_dpp v142, v142, v142 row_ror:4 row_mask:0xf bank_mask:0xf
	v_add_f32_dpp v143, v143, v143 row_ror:4 row_mask:0xf bank_mask:0xf
	v_add_f32_dpp v144, v144, v144 row_ror:4 row_mask:0xf bank_mask:0xf
	v_add_f32_dpp v145, v145, v145 row_ror:4 row_mask:0xf bank_mask:0xf
	v_add_f32_dpp v146, v146, v146 row_ror:4 row_mask:0xf bank_mask:0xf
	v_add_f32_dpp v147, v147, v147 row_ror:4 row_mask:0xf bank_mask:0xf
	v_add_f32_dpp v166, v166, v166 row_ror:4 row_mask:0xf bank_mask:0xf
	v_add_f32_dpp v140, v140, v140 row_ror:2 row_mask:0xf bank_mask:0xf
	v_add_f32_dpp v141, v141, v141 row_ror:2 row_mask:0xf bank_mask:0xf
	v_add_f32_dpp v142, v142, v142 row_ror:2 row_mask:0xf bank_mask:0xf
	v_add_f32_dpp v143, v143, v143 row_ror:2 row_mask:0xf bank_mask:0xf
	v_add_f32_dpp v144, v144, v144 row_ror:2 row_mask:0xf bank_mask:0xf
	v_add_f32_dpp v145, v145, v145 row_ror:2 row_mask:0xf bank_mask:0xf
	v_add_f32_dpp v146, v146, v146 row_ror:2 row_mask:0xf bank_mask:0xf
	v_add_f32_dpp v147, v147, v147 row_ror:2 row_mask:0xf bank_mask:0xf
	v_add_f32_dpp v166, v166, v166 row_ror:2 row_mask:0xf bank_mask:0xf
	v_add_f32_dpp v140, v140, v140 row_ror:1 row_mask:0xf bank_mask:0xf
	v_add_f32_dpp v141, v141, v141 row_ror:1 row_mask:0xf bank_mask:0xf
	v_add_f32_dpp v142, v142, v142 row_ror:1 row_mask:0xf bank_mask:0xf
	v_add_f32_dpp v143, v143, v143 row_ror:1 row_mask:0xf bank_mask:0xf
	v_add_f32_dpp v144, v144, v144 row_ror:1 row_mask:0xf bank_mask:0xf
	v_add_f32_dpp v145, v145, v145 row_ror:1 row_mask:0xf bank_mask:0xf
	v_add_f32_dpp v146, v146, v146 row_ror:1 row_mask:0xf bank_mask:0xf
	v_add_f32_dpp v147, v147, v147 row_ror:1 row_mask:0xf bank_mask:0xf
	v_add_f32_dpp v166, v166, v166 row_ror:1 row_mask:0xf bank_mask:0xf
	v_cvt_pk_f16_f32 v252, v140, v141
	v_cvt_pk_f16_f32 v253, v142, v143
	v_cvt_pk_f16_f32 v254, v144, v145
	v_cvt_pk_f16_f32 v255, v146, v147
	s_waitcnt lgkmcnt(0)
	v_add_f32_e32 v209, s12, v166
	v_add_u32_e32 v220, s18, v102
	v_add_u32_e32 v220, s18, v220
	v_min_u32_e32 v218, s19, v220
	v_lshlrev_b32_e32 v218, 9, v218
	v_lshl_add_u64 v[216:217], v[222:223], 0, v[218:219]
	global_load_dword v228, v[216:217], off nt
	global_load_dword v229, v[216:217], off offset:128 nt
	global_load_dword v230, v[216:217], off offset:256 nt
	global_load_dword v231, v[216:217], off offset:384 nt
	v_add_u32_e32 v220, s18, v220
	v_min_u32_e32 v218, s19, v220
	v_lshlrev_b32_e32 v218, 9, v218
	v_lshl_add_u64 v[216:217], v[222:223], 0, v[218:219]
	global_load_dword v232, v[216:217], off nt
	global_load_dword v233, v[216:217], off offset:128 nt
	global_load_dword v234, v[216:217], off offset:256 nt
	global_load_dword v235, v[216:217], off offset:384 nt
	v_add_u32_e32 v220, s18, v220
	v_min_u32_e32 v218, s19, v220
	v_lshlrev_b32_e32 v218, 9, v218
	v_lshl_add_u64 v[216:217], v[222:223], 0, v[218:219]
	global_load_dword v236, v[216:217], off nt
	global_load_dword v237, v[216:217], off offset:128 nt
	global_load_dword v238, v[216:217], off offset:256 nt
	global_load_dword v239, v[216:217], off offset:384 nt
	v_add_u32_e32 v220, s18, v220
	v_min_u32_e32 v218, s19, v220
	v_lshlrev_b32_e32 v218, 9, v218
	v_lshl_add_u64 v[216:217], v[222:223], 0, v[218:219]
	global_load_dword v240, v[216:217], off nt
	global_load_dword v241, v[216:217], off offset:128 nt
	global_load_dword v242, v[216:217], off offset:256 nt
	global_load_dword v243, v[216:217], off offset:384 nt
	v_add_u32_e32 v220, s18, v220
	v_min_u32_e32 v218, s19, v220
	v_lshlrev_b32_e32 v218, 9, v218
	v_lshl_add_u64 v[216:217], v[222:223], 0, v[218:219]
	global_load_dword v244, v[216:217], off nt
	global_load_dword v245, v[216:217], off offset:128 nt
	global_load_dword v246, v[216:217], off offset:256 nt
	global_load_dword v247, v[216:217], off offset:384 nt
	v_add_u32_e32 v220, s18, v220
	v_min_u32_e32 v218, s19, v220
	v_lshlrev_b32_e32 v218, 9, v218
	v_lshl_add_u64 v[216:217], v[222:223], 0, v[218:219]
	global_load_dword v248, v[216:217], off nt
	global_load_dword v249, v[216:217], off offset:128 nt
	global_load_dword v250, v[216:217], off offset:256 nt
	global_load_dword v251, v[216:217], off offset:384 nt
	s_waitcnt vmcnt(24)
